# speedup vs baseline: 1.0386x; 1.0386x over previous
_Z11prep_kernelPKfS0_S0_S0_S0_S0_S0_S0_S0_PKiPDv8_DF16bS4_PfS5_S5_PiPt:
	s_load_dwordx4 s[16:19], s[0:1], 0x0
	s_load_dwordx4 s[20:23], s[0:1], 0x10
	s_load_dwordx4 s[24:27], s[0:1], 0x20
	s_load_dwordx4 s[28:31], s[0:1], 0x30
	s_load_dwordx4 s[32:35], s[0:1], 0x40
	s_load_dwordx2 s[36:37], s[0:1], 0x80
	v_and_b32_e32 v126, 63, v0
	v_lshrrev_b32_e32 v128, 6, v0
	v_and_b32_e32 v1, 15, v0
	v_bfe_u32 v24, v0, 4, 2
	v_lshl_or_b32 v107, v128, 4, v1
	v_lshlrev_b32_e32 v106, 2, v107
	v_lshlrev_b32_e32 v127, 2, v0
	v_lshlrev_b32_e32 v25, 1, v107
	v_and_b32_e32 v26, 48, v0
	v_mul_u32_u24_e32 v27, 0x440, v24
	v_lshlrev_b32_e32 v120, 4, v0
	v_lshrrev_b32_e32 v58, 5, v0
	v_mul_u32_u24_e32 v58, 0x110, v58
	v_and_b32_e32 v125, 31, v0
	v_lshl_add_u32 v58, v125, 3, v58
	v_add_u32_e32 v124, 0x1b400, v58
	v_mul_u32_u24_e32 v52, 0x110, v1
	v_add_u32_e32 v52, v52, v26
	v_add_u32_e32 v53, 0x1b400, v52
	v_add_u32_e32 v54, 0x1c500, v52
	v_add_u32_e32 v55, v27, v25
	v_add_u32_e32 v55, 0x1c500, v55
	v_mul_u32_u24_e32 v56, 0x110, v107
	v_add_u32_e32 v56, v56, v26
	v_add_u32_e32 v57, 0x8800, v56
	s_lshl_b32 s12, s2, 4
	s_add_i32 s3, s12, 0xfffff800
	s_cmpk_gt_i32 s2, 0x7f
	s_cselect_b64 s[6:7], -1, 0
	s_mov_b32 s48, 0
	s_mov_b32 s49, -1
	v_lshl_or_b32 v123, s2, 3, v128
	v_lshlrev_b32_e32 v123, 12, v123
	v_lshl_add_u32 v123, v126, 4, v123
	s_waitcnt lgkmcnt(0)
	s_cmpk_lt_i32 s2, 0x80
	s_cselect_b32 s38, s16, s18
	s_cselect_b32 s39, s17, s19
	s_cselect_b32 s40, s20, s24
	s_cselect_b32 s41, s21, s25
	s_cselect_b32 s13, s12, s3
	s_cselect_b32 s44, 0x3db504f3, 1.0
	s_lshl_b32 s13, s13, 9
	s_add_u32 s38, s38, s13
	s_addc_u32 s39, s39, 0
	global_load_dwordx4 v[2:5], v120, s[38:39] nt
	s_and_b32 s13, s2, 7
	s_lshl_b32 s14, s13, 13
	v_add_u32_e32 v125, s14, v120
	global_load_dwordx4 v[80:83], v125, s[40:41]
	s_add_i32 s13, s2, 1
	s_and_b32 s13, s13, 7
	s_lshl_b32 s14, s13, 13
	v_add_u32_e32 v125, s14, v120
	global_load_dwordx4 v[84:87], v125, s[40:41]
	s_add_i32 s13, s2, 2
	s_and_b32 s13, s13, 7
	s_lshl_b32 s14, s13, 13
	v_add_u32_e32 v125, s14, v120
	global_load_dwordx4 v[88:91], v125, s[40:41]
	s_add_i32 s13, s2, 3
	s_and_b32 s13, s13, 7
	s_lshl_b32 s14, s13, 13
	v_add_u32_e32 v125, s14, v120
	global_load_dwordx4 v[92:95], v125, s[40:41]
	s_add_i32 s13, s2, 4
	s_and_b32 s13, s13, 7
	s_lshl_b32 s14, s13, 13
	v_add_u32_e32 v125, s14, v120
	global_load_dwordx4 v[96:99], v125, s[40:41]
	s_add_i32 s13, s2, 5
	s_and_b32 s13, s13, 7
	s_lshl_b32 s14, s13, 13
	v_add_u32_e32 v125, s14, v120
	global_load_dwordx4 v[100:103], v125, s[40:41]
	s_add_i32 s13, s2, 6
	s_and_b32 s13, s13, 7
	s_lshl_b32 s14, s13, 13
	v_add_u32_e32 v125, s14, v120
	global_load_dwordx4 v[108:111], v125, s[40:41]
	s_add_i32 s13, s2, 7
	s_and_b32 s13, s13, 7
	s_lshl_b32 s14, s13, 13
	v_add_u32_e32 v125, s14, v120
	global_load_dwordx4 v[112:115], v125, s[40:41]
	global_load_dword v129, v106, s[32:33]
	global_load_dword v130, v106, s[30:31]
	s_and_b64 vcc, exec, s[6:7]
	s_cbranch_vccz .Lp_q
	v_cmp_gt_u32_e32 vcc, 32, v126
	v_mov_b32_e32 v46, 0x3db504f3
	v_mov_b32_e32 v125, s22
	v_mov_b32_e32 v104, s26
	v_cndmask_b32_e32 v46, 1.0, v46, vcc
	v_cndmask_b32_e32 v104, v104, v125, vcc
	v_mov_b32_e32 v125, s23
	v_mov_b32_e32 v105, s27
	v_cndmask_b32_e32 v105, v105, v125, vcc
	v_and_b32_e32 v44, 31, v126
	v_lshlrev_b32_e32 v44, 4, v44
	v_mov_b32_e32 v45, 0
	v_lshl_add_u64 v[104:105], v[104:105], 0, v[44:45]
	global_load_dwordx4 v[116:119], v[104:105], off
	v_lshlrev_b32_e32 v121, 14, v128
	v_lshl_add_u32 v121, v126, 4, v121
	s_and_b32 s13, s2, 15
	s_lshl_b32 s14, s13, 10
	s_add_u32 s46, s28, s14
	s_addc_u32 s47, s29, 0
	global_load_dwordx4 v[132:135], v121, s[46:47]
	s_add_i32 s13, s2, 1
	s_and_b32 s13, s13, 15
	s_lshl_b32 s14, s13, 10
	s_add_u32 s46, s28, s14
	s_addc_u32 s47, s29, 0
	global_load_dwordx4 v[136:139], v121, s[46:47]
	s_add_i32 s13, s2, 2
	s_and_b32 s13, s13, 15
	s_lshl_b32 s14, s13, 10
	s_add_u32 s46, s28, s14
	s_addc_u32 s47, s29, 0
	global_load_dwordx4 v[140:143], v121, s[46:47]
	s_add_i32 s13, s2, 3
	s_and_b32 s13, s13, 15
	s_lshl_b32 s14, s13, 10
	s_add_u32 s46, s28, s14
	s_addc_u32 s47, s29, 0
	global_load_dwordx4 v[144:147], v121, s[46:47]
	s_add_i32 s13, s2, 4
	s_and_b32 s13, s13, 15
	s_lshl_b32 s14, s13, 10
	s_add_u32 s46, s28, s14
	s_addc_u32 s47, s29, 0
	global_load_dwordx4 v[148:151], v121, s[46:47]
	s_add_i32 s13, s2, 5
	s_and_b32 s13, s13, 15
	s_lshl_b32 s14, s13, 10
	s_add_u32 s46, s28, s14
	s_addc_u32 s47, s29, 0
	global_load_dwordx4 v[152:155], v121, s[46:47]
	s_add_i32 s13, s2, 6
	s_and_b32 s13, s13, 15
	s_lshl_b32 s14, s13, 10
	s_add_u32 s46, s28, s14
	s_addc_u32 s47, s29, 0
	global_load_dwordx4 v[156:159], v121, s[46:47]
	s_add_i32 s13, s2, 7
	s_and_b32 s13, s13, 15
	s_lshl_b32 s14, s13, 10
	s_add_u32 s46, s28, s14
	s_addc_u32 s47, s29, 0
	global_load_dwordx4 v[160:163], v121, s[46:47]
	s_add_i32 s13, s2, 8
	s_and_b32 s13, s13, 15
	s_lshl_b32 s14, s13, 10
	s_add_u32 s46, s28, s14
	s_addc_u32 s47, s29, 0
	global_load_dwordx4 v[28:31], v121, s[46:47]
	s_add_i32 s13, s2, 9
	s_and_b32 s13, s13, 15
	s_lshl_b32 s14, s13, 10
	s_add_u32 s46, s28, s14
	s_addc_u32 s47, s29, 0
	global_load_dwordx4 v[32:35], v121, s[46:47]
	s_add_i32 s13, s2, 10
	s_and_b32 s13, s13, 15
	s_lshl_b32 s14, s13, 10
	s_add_u32 s46, s28, s14
	s_addc_u32 s47, s29, 0
	global_load_dwordx4 v[36:39], v121, s[46:47]
	s_add_i32 s13, s2, 11
	s_and_b32 s13, s13, 15
	s_lshl_b32 s14, s13, 10
	s_add_u32 s46, s28, s14
	s_addc_u32 s47, s29, 0
	global_load_dwordx4 v[40:43], v121, s[46:47]
	s_add_i32 s13, s2, 12
	s_and_b32 s13, s13, 15
	s_lshl_b32 s14, s13, 10
	s_add_u32 s46, s28, s14
	s_addc_u32 s47, s29, 0
	global_load_dwordx4 v[60:63], v121, s[46:47]
	s_add_i32 s13, s2, 13
	s_and_b32 s13, s13, 15
	s_lshl_b32 s14, s13, 10
	s_add_u32 s46, s28, s14
	s_addc_u32 s47, s29, 0
	global_load_dwordx4 v[64:67], v121, s[46:47]
	s_add_i32 s13, s2, 14
	s_and_b32 s13, s13, 15
	s_lshl_b32 s14, s13, 10
	s_add_u32 s46, s28, s14
	s_addc_u32 s47, s29, 0
	global_load_dwordx4 v[68:71], v121, s[46:47]
	s_add_i32 s13, s2, 15
	s_and_b32 s13, s13, 15
	s_lshl_b32 s14, s13, 10
	s_add_u32 s46, s28, s14
	s_addc_u32 s47, s29, 0
	global_load_dwordx4 v[72:75], v121, s[46:47]
	v_mul_u32_u24_e32 v59, 0x1040, v128
	v_lshl_add_u32 v59, v126, 2, v59
	v_add_u32_e32 v59, 0x11000, v59
	v_mul_u32_u24_e32 v76, 0x1100, v128
	v_lshl_add_u32 v76, v126, 3, v76
	v_add_u32_e32 v76, 0x8700, v76
	v_lshrrev_b32_e32 v77, 2, v126
	v_mul_u32_u24_e32 v77, 0x104, v77
	v_mul_u32_u24_e32 v125, 0x1040, v128
	v_add_u32_e32 v77, v77, v125
	v_and_b32_e32 v125, 3, v126
	v_lshl_add_u32 v77, v125, 6, v77
	v_add_u32_e32 v77, 0x11000, v77
	s_waitcnt vmcnt(27)
	v_cvt_pk_bf16_f32 v12, v2, v3
	v_cvt_pk_bf16_f32 v13, v4, v5
	ds_write_b64 v124, v[12:13]
	s_waitcnt vmcnt(26)
	v_cvt_pk_bf16_f32 v6, v80, v81
	v_cvt_pk_bf16_f32 v7, v82, v83
	s_and_b32 s13, s2, 7
	s_mul_i32 s14, s13, 0x1100
	v_add_u32_e32 v125, s14, v58
	ds_write_b64 v125, v[6:7]
	s_waitcnt vmcnt(25)
	v_cvt_pk_bf16_f32 v8, v84, v85
	v_cvt_pk_bf16_f32 v9, v86, v87
	s_add_i32 s13, s2, 1
	s_and_b32 s13, s13, 7
	s_mul_i32 s14, s13, 0x1100
	v_add_u32_e32 v10, s14, v58
	ds_write_b64 v10, v[8:9]
	s_waitcnt vmcnt(24)
	v_cvt_pk_bf16_f32 v6, v88, v89
	v_cvt_pk_bf16_f32 v7, v90, v91
	s_add_i32 s13, s2, 2
	s_and_b32 s13, s13, 7
	s_mul_i32 s14, s13, 0x1100
	v_add_u32_e32 v125, s14, v58
	ds_write_b64 v125, v[6:7]
	s_waitcnt vmcnt(23)
	v_cvt_pk_bf16_f32 v8, v92, v93
	v_cvt_pk_bf16_f32 v9, v94, v95
	s_add_i32 s13, s2, 3
	s_and_b32 s13, s13, 7
	s_mul_i32 s14, s13, 0x1100
	v_add_u32_e32 v10, s14, v58
	ds_write_b64 v10, v[8:9]
	s_waitcnt vmcnt(22)
	v_cvt_pk_bf16_f32 v6, v96, v97
	v_cvt_pk_bf16_f32 v7, v98, v99
	s_add_i32 s13, s2, 4
	s_and_b32 s13, s13, 7
	s_mul_i32 s14, s13, 0x1100
	v_add_u32_e32 v125, s14, v58
	ds_write_b64 v125, v[6:7]
	s_waitcnt vmcnt(21)
	v_cvt_pk_bf16_f32 v8, v100, v101
	v_cvt_pk_bf16_f32 v9, v102, v103
	s_add_i32 s13, s2, 5
	s_and_b32 s13, s13, 7
	s_mul_i32 s14, s13, 0x1100
	v_add_u32_e32 v10, s14, v58
	ds_write_b64 v10, v[8:9]
	s_waitcnt vmcnt(20)
	v_cvt_pk_bf16_f32 v6, v108, v109
	v_cvt_pk_bf16_f32 v7, v110, v111
	s_add_i32 s13, s2, 6
	s_and_b32 s13, s13, 7
	s_mul_i32 s14, s13, 0x1100
	v_add_u32_e32 v125, s14, v58
	ds_write_b64 v125, v[6:7]
	s_waitcnt vmcnt(19)
	v_cvt_pk_bf16_f32 v8, v112, v113
	v_cvt_pk_bf16_f32 v9, v114, v115
	s_add_i32 s13, s2, 7
	s_and_b32 s13, s13, 7
	s_mul_i32 s14, s13, 0x1100
	v_add_u32_e32 v10, s14, v58
	ds_write_b64 v10, v[8:9]
	s_waitcnt vmcnt(16)
	v_pk_mul_f32 v[116:117], v[46:47], v[116:117] op_sel_hi:[0,1]
	v_pk_mul_f32 v[118:119], v[46:47], v[118:119] op_sel_hi:[0,1]
	s_waitcnt vmcnt(15)
	v_mul_f32_e32 v6, v117, v133
	v_mul_f32_e32 v7, v119, v135
	v_fmac_f32_e32 v6, v116, v132
	v_fmac_f32_e32 v7, v118, v134
	s_and_b32 s13, s2, 15
	s_mul_i32 s14, s13, 0x104
	s_mul_i32 s15, s13, 0x110
	v_add_f32_e32 v6, v6, v7
	v_add_u32_e32 v125, s14, v59
	ds_write_b32 v125, v6
	v_cvt_pk_bf16_f32 v8, v132, v133
	v_cvt_pk_bf16_f32 v9, v134, v135
	v_add_u32_e32 v10, s15, v76
	s_mov_b64 exec, s[48:49]
	ds_write_b64 v10, v[8:9]
	s_mov_b64 exec, -1
	s_waitcnt vmcnt(14)
	v_mul_f32_e32 v11, v117, v137
	v_mul_f32_e32 v15, v119, v139
	v_fmac_f32_e32 v11, v116, v136
	v_fmac_f32_e32 v15, v118, v138
	s_add_i32 s13, s2, 1
	s_and_b32 s13, s13, 15
	s_mul_i32 s14, s13, 0x104
	s_mul_i32 s15, s13, 0x110
	v_add_f32_e32 v11, v11, v15
	v_add_u32_e32 v16, s14, v59
	ds_write_b32 v16, v11
	v_cvt_pk_bf16_f32 v12, v136, v137
	v_cvt_pk_bf16_f32 v13, v138, v139
	v_add_u32_e32 v14, s15, v76
	s_mov_b64 exec, s[48:49]
	ds_write_b64 v14, v[12:13]
	s_mov_b64 exec, -1
	s_waitcnt vmcnt(13)
	v_mul_f32_e32 v6, v117, v141
	v_mul_f32_e32 v7, v119, v143
	v_fmac_f32_e32 v6, v116, v140
	v_fmac_f32_e32 v7, v118, v142
	s_add_i32 s13, s2, 2
	s_and_b32 s13, s13, 15
	s_mul_i32 s14, s13, 0x104
	s_mul_i32 s15, s13, 0x110
	v_add_f32_e32 v6, v6, v7
	v_add_u32_e32 v125, s14, v59
	ds_write_b32 v125, v6
	v_cvt_pk_bf16_f32 v8, v140, v141
	v_cvt_pk_bf16_f32 v9, v142, v143
	v_add_u32_e32 v10, s15, v76
	s_mov_b64 exec, s[48:49]
	ds_write_b64 v10, v[8:9]
	s_mov_b64 exec, -1
	s_waitcnt vmcnt(12)
	v_mul_f32_e32 v11, v117, v145
	v_mul_f32_e32 v15, v119, v147
	v_fmac_f32_e32 v11, v116, v144
	v_fmac_f32_e32 v15, v118, v146
	s_add_i32 s13, s2, 3
	s_and_b32 s13, s13, 15
	s_mul_i32 s14, s13, 0x104
	s_mul_i32 s15, s13, 0x110
	v_add_f32_e32 v11, v11, v15
	v_add_u32_e32 v16, s14, v59
	ds_write_b32 v16, v11
	v_cvt_pk_bf16_f32 v12, v144, v145
	v_cvt_pk_bf16_f32 v13, v146, v147
	v_add_u32_e32 v14, s15, v76
	s_mov_b64 exec, s[48:49]
	ds_write_b64 v14, v[12:13]
	s_mov_b64 exec, -1
	s_waitcnt vmcnt(11)
	v_mul_f32_e32 v6, v117, v149
	v_mul_f32_e32 v7, v119, v151
	v_fmac_f32_e32 v6, v116, v148
	v_fmac_f32_e32 v7, v118, v150
	s_add_i32 s13, s2, 4
	s_and_b32 s13, s13, 15
	s_mul_i32 s14, s13, 0x104
	s_mul_i32 s15, s13, 0x110
	v_add_f32_e32 v6, v6, v7
	v_add_u32_e32 v125, s14, v59
	ds_write_b32 v125, v6
	v_cvt_pk_bf16_f32 v8, v148, v149
	v_cvt_pk_bf16_f32 v9, v150, v151
	v_add_u32_e32 v10, s15, v76
	s_mov_b64 exec, s[48:49]
	ds_write_b64 v10, v[8:9]
	s_mov_b64 exec, -1
	s_waitcnt vmcnt(10)
	v_mul_f32_e32 v11, v117, v153
	v_mul_f32_e32 v15, v119, v155
	v_fmac_f32_e32 v11, v116, v152
	v_fmac_f32_e32 v15, v118, v154
	s_add_i32 s13, s2, 5
	s_and_b32 s13, s13, 15
	s_mul_i32 s14, s13, 0x104
	s_mul_i32 s15, s13, 0x110
	v_add_f32_e32 v11, v11, v15
	v_add_u32_e32 v16, s14, v59
	ds_write_b32 v16, v11
	v_cvt_pk_bf16_f32 v12, v152, v153
	v_cvt_pk_bf16_f32 v13, v154, v155
	v_add_u32_e32 v14, s15, v76
	s_mov_b64 exec, s[48:49]
	ds_write_b64 v14, v[12:13]
	s_mov_b64 exec, -1
	s_waitcnt vmcnt(9)
	v_mul_f32_e32 v6, v117, v157
	v_mul_f32_e32 v7, v119, v159
	v_fmac_f32_e32 v6, v116, v156
	v_fmac_f32_e32 v7, v118, v158
	s_add_i32 s13, s2, 6
	s_and_b32 s13, s13, 15
	s_mul_i32 s14, s13, 0x104
	s_mul_i32 s15, s13, 0x110
	v_add_f32_e32 v6, v6, v7
	v_add_u32_e32 v125, s14, v59
	ds_write_b32 v125, v6
	v_cvt_pk_bf16_f32 v8, v156, v157
	v_cvt_pk_bf16_f32 v9, v158, v159
	v_add_u32_e32 v10, s15, v76
	s_mov_b64 exec, s[48:49]
	ds_write_b64 v10, v[8:9]
	s_mov_b64 exec, -1
	s_waitcnt vmcnt(8)
	v_mul_f32_e32 v11, v117, v161
	v_mul_f32_e32 v15, v119, v163
	v_fmac_f32_e32 v11, v116, v160
	v_fmac_f32_e32 v15, v118, v162
	s_add_i32 s13, s2, 7
	s_and_b32 s13, s13, 15
	s_mul_i32 s14, s13, 0x104
	s_mul_i32 s15, s13, 0x110
	v_add_f32_e32 v11, v11, v15
	v_add_u32_e32 v16, s14, v59
	ds_write_b32 v16, v11
	v_cvt_pk_bf16_f32 v12, v160, v161
	v_cvt_pk_bf16_f32 v13, v162, v163
	v_add_u32_e32 v14, s15, v76
	s_mov_b64 exec, s[48:49]
	ds_write_b64 v14, v[12:13]
	s_mov_b64 exec, -1
	s_waitcnt vmcnt(7)
	v_mul_f32_e32 v6, v117, v29
	v_mul_f32_e32 v7, v119, v31
	v_fmac_f32_e32 v6, v116, v28
	v_fmac_f32_e32 v7, v118, v30
	s_add_i32 s13, s2, 8
	s_and_b32 s13, s13, 15
	s_mul_i32 s14, s13, 0x104
	s_mul_i32 s15, s13, 0x110
	v_add_f32_e32 v6, v6, v7
	v_add_u32_e32 v125, s14, v59
	ds_write_b32 v125, v6
	v_cvt_pk_bf16_f32 v8, v28, v29
	v_cvt_pk_bf16_f32 v9, v30, v31
	v_add_u32_e32 v10, s15, v76
	s_mov_b64 exec, s[48:49]
	ds_write_b64 v10, v[8:9]
	s_mov_b64 exec, -1
	s_waitcnt vmcnt(6)
	v_mul_f32_e32 v11, v117, v33
	v_mul_f32_e32 v15, v119, v35
	v_fmac_f32_e32 v11, v116, v32
	v_fmac_f32_e32 v15, v118, v34
	s_add_i32 s13, s2, 9
	s_and_b32 s13, s13, 15
	s_mul_i32 s14, s13, 0x104
	s_mul_i32 s15, s13, 0x110
	v_add_f32_e32 v11, v11, v15
	v_add_u32_e32 v16, s14, v59
	ds_write_b32 v16, v11
	v_cvt_pk_bf16_f32 v12, v32, v33
	v_cvt_pk_bf16_f32 v13, v34, v35
	v_add_u32_e32 v14, s15, v76
	s_mov_b64 exec, s[48:49]
	ds_write_b64 v14, v[12:13]
	s_mov_b64 exec, -1
	s_waitcnt vmcnt(5)
	v_mul_f32_e32 v6, v117, v37
	v_mul_f32_e32 v7, v119, v39
	v_fmac_f32_e32 v6, v116, v36
	v_fmac_f32_e32 v7, v118, v38
	s_add_i32 s13, s2, 10
	s_and_b32 s13, s13, 15
	s_mul_i32 s14, s13, 0x104
	s_mul_i32 s15, s13, 0x110
	v_add_f32_e32 v6, v6, v7
	v_add_u32_e32 v125, s14, v59
	ds_write_b32 v125, v6
	v_cvt_pk_bf16_f32 v8, v36, v37
	v_cvt_pk_bf16_f32 v9, v38, v39
	v_add_u32_e32 v10, s15, v76
	s_mov_b64 exec, s[48:49]
	ds_write_b64 v10, v[8:9]
	s_mov_b64 exec, -1
	s_waitcnt vmcnt(4)
	v_mul_f32_e32 v11, v117, v41
	v_mul_f32_e32 v15, v119, v43
	v_fmac_f32_e32 v11, v116, v40
	v_fmac_f32_e32 v15, v118, v42
	s_add_i32 s13, s2, 11
	s_and_b32 s13, s13, 15
	s_mul_i32 s14, s13, 0x104
	s_mul_i32 s15, s13, 0x110
	v_add_f32_e32 v11, v11, v15
	v_add_u32_e32 v16, s14, v59
	ds_write_b32 v16, v11
	v_cvt_pk_bf16_f32 v12, v40, v41
	v_cvt_pk_bf16_f32 v13, v42, v43
	v_add_u32_e32 v14, s15, v76
	s_mov_b64 exec, s[48:49]
	ds_write_b64 v14, v[12:13]
	s_mov_b64 exec, -1
	s_waitcnt vmcnt(3)
	v_mul_f32_e32 v6, v117, v61
	v_mul_f32_e32 v7, v119, v63
	v_fmac_f32_e32 v6, v116, v60
	v_fmac_f32_e32 v7, v118, v62
	s_add_i32 s13, s2, 12
	s_and_b32 s13, s13, 15
	s_mul_i32 s14, s13, 0x104
	s_mul_i32 s15, s13, 0x110
	v_add_f32_e32 v6, v6, v7
	v_add_u32_e32 v125, s14, v59
	ds_write_b32 v125, v6
	v_cvt_pk_bf16_f32 v8, v60, v61
	v_cvt_pk_bf16_f32 v9, v62, v63
	v_add_u32_e32 v10, s15, v76
	s_mov_b64 exec, s[48:49]
	ds_write_b64 v10, v[8:9]
	s_mov_b64 exec, -1
	s_waitcnt vmcnt(2)
	v_mul_f32_e32 v11, v117, v65
	v_mul_f32_e32 v15, v119, v67
	v_fmac_f32_e32 v11, v116, v64
	v_fmac_f32_e32 v15, v118, v66
	s_add_i32 s13, s2, 13
	s_and_b32 s13, s13, 15
	s_mul_i32 s14, s13, 0x104
	s_mul_i32 s15, s13, 0x110
	v_add_f32_e32 v11, v11, v15
	v_add_u32_e32 v16, s14, v59
	ds_write_b32 v16, v11
	v_cvt_pk_bf16_f32 v12, v64, v65
	v_cvt_pk_bf16_f32 v13, v66, v67
	v_add_u32_e32 v14, s15, v76
	s_mov_b64 exec, s[48:49]
	ds_write_b64 v14, v[12:13]
	s_mov_b64 exec, -1
	s_waitcnt vmcnt(1)
	v_mul_f32_e32 v6, v117, v69
	v_mul_f32_e32 v7, v119, v71
	v_fmac_f32_e32 v6, v116, v68
	v_fmac_f32_e32 v7, v118, v70
	s_add_i32 s13, s2, 14
	s_and_b32 s13, s13, 15
	s_mul_i32 s14, s13, 0x104
	s_mul_i32 s15, s13, 0x110
	v_add_f32_e32 v6, v6, v7
	v_add_u32_e32 v125, s14, v59
	ds_write_b32 v125, v6
	v_cvt_pk_bf16_f32 v8, v68, v69
	v_cvt_pk_bf16_f32 v9, v70, v71
	v_add_u32_e32 v10, s15, v76
	s_mov_b64 exec, s[48:49]
	ds_write_b64 v10, v[8:9]
	s_mov_b64 exec, -1
	s_waitcnt vmcnt(0)
	v_mul_f32_e32 v11, v117, v73
	v_mul_f32_e32 v15, v119, v75
	v_fmac_f32_e32 v11, v116, v72
	v_fmac_f32_e32 v15, v118, v74
	s_add_i32 s13, s2, 15
	s_and_b32 s13, s13, 15
	s_mul_i32 s14, s13, 0x104
	s_mul_i32 s15, s13, 0x110
	v_add_f32_e32 v11, v11, v15
	v_add_u32_e32 v16, s14, v59
	ds_write_b32 v16, v11
	v_cvt_pk_bf16_f32 v12, v72, v73
	v_cvt_pk_bf16_f32 v13, v74, v75
	v_add_u32_e32 v14, s15, v76
	s_mov_b64 exec, s[48:49]
	ds_write_b64 v14, v[12:13]
	s_mov_b64 exec, -1
	s_waitcnt lgkmcnt(0)
	ds_read2_b32 v[60:61], v77 offset0:0 offset1:1
	ds_read2_b32 v[62:63], v77 offset0:2 offset1:3
	ds_read2_b32 v[64:65], v77 offset0:4 offset1:5
	ds_read2_b32 v[66:67], v77 offset0:6 offset1:7
	ds_read2_b32 v[68:69], v77 offset0:8 offset1:9
	ds_read2_b32 v[70:71], v77 offset0:10 offset1:11
	ds_read2_b32 v[72:73], v77 offset0:12 offset1:13
	ds_read2_b32 v[74:75], v77 offset0:14 offset1:15
	s_waitcnt lgkmcnt(0)
	v_add_f32_e32 v78, 0, v60
	v_add_f32_e32 v78, v78, v61
	v_add_f32_e32 v78, v78, v62
	v_add_f32_e32 v78, v78, v63
	v_add_f32_e32 v78, v78, v64
	v_add_f32_e32 v78, v78, v65
	v_add_f32_e32 v78, v78, v66
	v_add_f32_e32 v78, v78, v67
	v_add_f32_e32 v78, v78, v68
	v_add_f32_e32 v78, v78, v69
	v_add_f32_e32 v78, v78, v70
	v_add_f32_e32 v78, v78, v71
	v_add_f32_e32 v78, v78, v72
	v_add_f32_e32 v78, v78, v73
	v_add_f32_e32 v78, v78, v74
	v_add_f32_e32 v78, v78, v75
	s_nop 1
	v_add_f32_dpp v78, v78, v78 quad_perm:[1,0,3,2] row_mask:0xf bank_mask:0xf bound_ctrl:1
	s_nop 1
	v_add_f32_dpp v78, v78, v78 quad_perm:[2,3,0,1] row_mask:0xf bank_mask:0xf bound_ctrl:1
	v_lshlrev_b32_e32 v79, 4, v1
	ds_bpermute_b32 v78, v79, v78
	s_waitcnt lgkmcnt(0)
	s_barrier
	ds_read_b128 v[28:31], v53
	ds_read_b128 v[60:63], v56
	ds_read_b128 v[32:35], v53 offset:64
	ds_read_b128 v[64:67], v56 offset:64
	ds_read_b128 v[36:39], v53 offset:128
	ds_read_b128 v[68:71], v56 offset:128
	ds_read_b128 v[40:43], v53 offset:192
	ds_read_b128 v[72:75], v56 offset:192
	s_waitcnt lgkmcnt(6)
	v_mfma_f32_16x16x32_bf16 v[18:21], v[28:31], v[60:63], 0
	s_waitcnt lgkmcnt(4)
	v_mfma_f32_16x16x32_bf16 v[18:21], v[32:35], v[64:67], v[18:21]
	s_waitcnt lgkmcnt(2)
	v_mfma_f32_16x16x32_bf16 v[18:21], v[36:39], v[68:71], v[18:21]
	s_waitcnt lgkmcnt(0)
	v_mfma_f32_16x16x32_bf16 v[18:21], v[40:43], v[72:75], v[18:21]
	s_nop 7
	v_mul_f32_e32 v18, s44, v18
	v_mul_f32_e32 v19, s44, v19
	v_mul_f32_e32 v20, s44, v20
	v_mul_f32_e32 v21, s44, v21
	v_cvt_pk_bf16_f32 v18, v18, v18
	v_cvt_pk_bf16_f32 v19, v19, v19
	v_cvt_pk_bf16_f32 v20, v20, v20
	v_cvt_pk_bf16_f32 v21, v21, v21
	ds_write_b16 v55, v18
	ds_write_b16 v55, v19 offset:272
	ds_write_b16 v55, v20 offset:544
	ds_write_b16 v55, v21 offset:816
	s_waitcnt lgkmcnt(0)
	s_barrier
	ds_read_b128 v[28:31], v54
	ds_read_b128 v[60:63], v57
	ds_read_b128 v[32:35], v54 offset:64
	ds_read_b128 v[64:67], v57 offset:64
	ds_read_b128 v[36:39], v54 offset:128
	ds_read_b128 v[68:71], v57 offset:128
	ds_read_b128 v[40:43], v54 offset:192
	ds_read_b128 v[72:75], v57 offset:192
	s_waitcnt lgkmcnt(6)
	v_mfma_f32_16x16x32_bf16 v[18:21], v[28:31], v[60:63], 0
	s_waitcnt lgkmcnt(4)
	v_mfma_f32_16x16x32_bf16 v[18:21], v[32:35], v[64:67], v[18:21]
	s_waitcnt lgkmcnt(2)
	v_mfma_f32_16x16x32_bf16 v[18:21], v[36:39], v[68:71], v[18:21]
	s_waitcnt lgkmcnt(0)
	v_mfma_f32_16x16x32_bf16 v[18:21], v[40:43], v[72:75], v[18:21]
	s_nop 2
	v_mov_b32_e32 v28, v78
	s_load_dwordx2 s[4:5], s[0:1], 0x70
	v_lshl_or_b32 v30, v24, 2, s3
	v_ashrrev_i32_e32 v31, 31, v30
	v_mov_b32_e32 v107, 0
	s_waitcnt lgkmcnt(0)
	v_add_f32_e32 v34, v130, v28
	v_add_f32_e32 v35, v34, v18
	v_add_f32_e32 v28, v35, v35
	v_mul_f32_e32 v28, 0x3fb8aa3b, v28
	v_exp_f32_e32 v32, v28
	v_lshlrev_b64 v[28:29], 9, v[30:31]
	s_mov_b32 s8, 0x19200
	v_add3_u32 v37, v27, v25, s8
	v_add_f32_e32 v31, 1.0, v32
	v_rcp_f32_e32 v31, v31
	v_lshl_add_u64 v[32:33], s[4:5], 0, v[106:107]
	v_lshl_add_u64 v[28:29], v[32:33], 0, v[28:29]
	global_store_dword v[28:29], v35, off sc1
	v_fma_f32 v35, v31, -2.0, 1.0
	v_fma_f32 v28, -v35, v35, 1.0
	v_mul_f32_e32 v28, v129, v28
	v_add_f32_e32 v31, v34, v19
	v_cvt_pk_bf16_f32 v29, v28, s0
	v_mul_f32_e64 v27, v35, -v28
	v_add_f32_e32 v28, v31, v31
	v_mul_f32_e32 v28, 0x3fb8aa3b, v28
	v_exp_f32_e32 v38, v28
	v_cvt_pk_bf16_f32 v27, v27, s0
	ds_write_b16 v37, v27 offset:4352
	v_or_b32_e32 v28, 1, v30
	v_add_f32_e32 v27, 1.0, v38
	v_rcp_f32_e32 v27, v27
	ds_write_b16 v37, v29
	v_ashrrev_i32_e32 v29, 31, v28
	v_lshlrev_b64 v[28:29], 9, v[28:29]
	v_lshl_add_u64 v[28:29], v[32:33], 0, v[28:29]
	v_fma_f32 v27, v27, -2.0, 1.0
	global_store_dword v[28:29], v31, off sc1
	v_fma_f32 v28, -v27, v27, 1.0
	v_mul_f32_e32 v28, v129, v28
	v_cvt_pk_bf16_f32 v29, v28, s0
	v_add_f32_e32 v31, v34, v20
	ds_write_b16 v37, v29 offset:272
	v_add_f32_e32 v29, v31, v31
	v_mul_f32_e32 v29, 0x3fb8aa3b, v29
	v_exp_f32_e32 v38, v29
	v_mul_f32_e64 v28, v27, -v28
	v_cvt_pk_bf16_f32 v28, v28, s0
	ds_write_b16 v37, v28 offset:4624
	v_add_f32_e32 v38, 1.0, v38
	v_or_b32_e32 v28, 2, v30
	v_rcp_f32_e32 v38, v38
	v_ashrrev_i32_e32 v29, 31, v28
	v_lshlrev_b64 v[28:29], 9, v[28:29]
	v_lshl_add_u64 v[28:29], v[32:33], 0, v[28:29]
	global_store_dword v[28:29], v31, off sc1
	v_fma_f32 v28, v38, -2.0, 1.0
	v_fma_f32 v29, -v28, v28, 1.0
	v_mul_f32_e32 v29, v129, v29
	v_cvt_pk_bf16_f32 v31, v29, s0
	v_add_f32_e32 v34, v34, v21
	ds_write_b16 v37, v31 offset:544
	v_add_f32_e32 v31, v34, v34
	v_mul_f32_e32 v31, 0x3fb8aa3b, v31
	v_exp_f32_e32 v38, v31
	v_mul_f32_e64 v29, v28, -v29
	v_cvt_pk_bf16_f32 v29, v29, s0
	ds_write_b16 v37, v29 offset:4896
	v_add_f32_e32 v29, 1.0, v38
	v_rcp_f32_e32 v29, v29
	v_or_b32_e32 v30, 3, v30
	v_ashrrev_i32_e32 v31, 31, v30
	v_lshlrev_b64 v[30:31], 9, v[30:31]
	v_lshl_add_u64 v[30:31], v[32:33], 0, v[30:31]
	v_fma_f32 v29, v29, -2.0, 1.0
	global_store_dword v[30:31], v34, off sc1
	v_fma_f32 v30, -v29, v29, 1.0
	v_mul_f32_e32 v30, v129, v30
	v_cvt_pk_bf16_f32 v31, v30, s0
	v_mul_f32_e64 v30, v29, -v30
	v_cvt_pk_bf16_f32 v30, v30, s0
	ds_write_b16 v37, v30 offset:5168
	v_mov_b32_e32 v30, 0x1d800
	v_mul_f32_e32 v36, v129, v35
	v_lshl_or_b32 v32, v128, 6, v30
	v_mov_b32_e32 v30, v107
	ds_write_b16 v37, v31 offset:816
	v_mov_b32_e32 v31, 0
	v_mov_b32_dpp v30, v36 quad_perm:[1,0,3,2] row_mask:0xf bank_mask:0xf
	v_fmac_f32_e32 v30, v129, v35
	v_cmp_eq_u32_e32 vcc, 0, v1
	v_add_u32_e32 v26, v32, v26
	v_add_f32_dpp v30, v30, v30 quad_perm:[2,3,0,1] row_mask:0xf bank_mask:0xf bound_ctrl:1
	s_nop 1
	v_add_f32_dpp v30, v30, v30 row_half_mirror row_mask:0xf bank_mask:0xf bound_ctrl:1
	s_nop 1
	v_mov_b32_dpp v31, v30 row_mirror row_mask:0xf bank_mask:0xf
	s_and_saveexec_b64 s[4:5], vcc
	v_add_f32_e32 v30, v30, v31
	ds_write_b32 v26, v30
	s_or_b64 exec, exec, s[4:5]
	v_mul_f32_e32 v30, v129, v27
	v_mov_b32_e32 v31, 0
	s_nop 1
	v_mov_b32_dpp v31, v30 quad_perm:[1,0,3,2] row_mask:0xf bank_mask:0xf
	v_fmac_f32_e32 v31, v129, v27
	s_nop 1
	v_add_f32_dpp v27, v31, v31 quad_perm:[2,3,0,1] row_mask:0xf bank_mask:0xf bound_ctrl:1
	s_nop 1
	v_add_f32_dpp v27, v27, v27 row_half_mirror row_mask:0xf bank_mask:0xf bound_ctrl:1
	s_nop 1
	v_mov_b32_dpp v107, v27 row_mirror row_mask:0xf bank_mask:0xf
	s_and_saveexec_b64 s[4:5], vcc
	v_add_f32_e32 v27, v27, v107
	ds_write_b32 v26, v27 offset:4
	s_or_b64 exec, exec, s[4:5]
	v_mul_f32_e32 v30, v129, v28
	v_mov_b32_e32 v31, 0
	v_mov_b32_e32 v27, 0
	s_nop 0
	v_mov_b32_dpp v31, v30 quad_perm:[1,0,3,2] row_mask:0xf bank_mask:0xf
	v_fmac_f32_e32 v31, v129, v28
	v_mov_b32_e32 v30, 0
	s_nop 0
	v_add_f32_dpp v28, v31, v31 quad_perm:[2,3,0,1] row_mask:0xf bank_mask:0xf bound_ctrl:1
	s_nop 1
	v_add_f32_dpp v28, v28, v28 row_half_mirror row_mask:0xf bank_mask:0xf bound_ctrl:1
	s_nop 1
	v_mov_b32_dpp v30, v28 row_mirror row_mask:0xf bank_mask:0xf
	s_and_saveexec_b64 s[4:5], vcc
	v_add_f32_e32 v28, v28, v30
	ds_write_b32 v26, v28 offset:8
	s_or_b64 exec, exec, s[4:5]
	v_mul_f32_e32 v28, v129, v29
	v_mov_b32_e32 v30, 0
	s_nop 1
	v_mov_b32_dpp v30, v28 quad_perm:[1,0,3,2] row_mask:0xf bank_mask:0xf
	v_fmac_f32_e32 v30, v129, v29
	s_nop 1
	v_add_f32_dpp v28, v30, v30 quad_perm:[2,3,0,1] row_mask:0xf bank_mask:0xf bound_ctrl:1
	s_nop 1
	v_add_f32_dpp v28, v28, v28 row_half_mirror row_mask:0xf bank_mask:0xf bound_ctrl:1
	s_nop 1
	v_mov_b32_dpp v27, v28 row_mirror row_mask:0xf bank_mask:0xf
	s_and_saveexec_b64 s[4:5], vcc
	v_add_f32_e32 v27, v28, v27
	ds_write_b32 v26, v27 offset:12
	s_or_b64 exec, exec, s[4:5]
	s_mov_b64 s[4:5], 0
	s_branch .LBB0_28

	.amdhsa_kernel _Z11prep_kernelPKfS0_S0_S0_S0_S0_S0_S0_S0_PKiPDv8_DF16bS4_PfS5_S5_PiPt
		.amdhsa_group_segment_fixed_size 121344
		.amdhsa_private_segment_fixed_size 0
		.amdhsa_kernarg_size 136
		.amdhsa_user_sgpr_count 2
		.amdhsa_user_sgpr_dispatch_ptr 0
		.amdhsa_user_sgpr_queue_ptr 0
		.amdhsa_user_sgpr_kernarg_segment_ptr 1
		.amdhsa_user_sgpr_dispatch_id 0
		.amdhsa_user_sgpr_kernarg_preload_length 0
		.amdhsa_user_sgpr_kernarg_preload_offset 0
		.amdhsa_user_sgpr_private_segment_size 0
		.amdhsa_uses_dynamic_stack 0
		.amdhsa_enable_private_segment 0
		.amdhsa_system_sgpr_workgroup_id_x 1
		.amdhsa_system_sgpr_workgroup_id_y 0
		.amdhsa_system_sgpr_workgroup_id_z 0
		.amdhsa_system_sgpr_workgroup_info 0
		.amdhsa_system_vgpr_workitem_id 0
		.amdhsa_next_free_vgpr 164
		.amdhsa_next_free_sgpr 96
		.amdhsa_accum_offset 164
		.amdhsa_reserve_vcc 1
		.amdhsa_float_round_mode_32 0
		.amdhsa_float_round_mode_16_64 0
		.amdhsa_float_denorm_mode_32 3
		.amdhsa_float_denorm_mode_16_64 3
		.amdhsa_dx10_clamp 1
		.amdhsa_ieee_mode 1
		.amdhsa_fp16_overflow 0
		.amdhsa_tg_split 0
		.amdhsa_exception_fp_ieee_invalid_op 0
		.amdhsa_exception_fp_denorm_src 0
		.amdhsa_exception_fp_ieee_div_zero 0
		.amdhsa_exception_fp_ieee_overflow 0
		.amdhsa_exception_fp_ieee_underflow 0
		.amdhsa_exception_fp_ieee_inexact 0
		.amdhsa_exception_int_div_zero 0
	.end_amdhsa_kernel

amdhsa.kernels:
  - .agpr_count:     0
    .args:
      - .actual_access:  read_only
        .address_space:  global
        .offset:         0
        .size:           8
        .value_kind:     global_buffer
      - .actual_access:  read_only
        .address_space:  global
        .offset:         8
        .size:           8
        .value_kind:     global_buffer
      - .actual_access:  read_only
        .address_space:  global
        .offset:         16
        .size:           8
        .value_kind:     global_buffer
      - .actual_access:  read_only
        .address_space:  global
        .offset:         24
        .size:           8
        .value_kind:     global_buffer
      - .actual_access:  read_only
        .address_space:  global
        .offset:         32
        .size:           8
        .value_kind:     global_buffer
      - .actual_access:  read_only
        .address_space:  global
        .offset:         40
        .size:           8
        .value_kind:     global_buffer
      - .actual_access:  read_only
        .address_space:  global
        .offset:         48
        .size:           8
        .value_kind:     global_buffer
      - .actual_access:  read_only
        .address_space:  global
        .offset:         56
        .size:           8
        .value_kind:     global_buffer
      - .actual_access:  read_only
        .address_space:  global
        .offset:         64
        .size:           8
        .value_kind:     global_buffer
      - .actual_access:  read_only
        .address_space:  global
        .offset:         72
        .size:           8
        .value_kind:     global_buffer
      - .actual_access:  write_only
        .address_space:  global
        .offset:         80
        .size:           8
        .value_kind:     global_buffer
      - .actual_access:  write_only
        .address_space:  global
        .offset:         88
        .size:           8
        .value_kind:     global_buffer
      - .actual_access:  write_only
        .address_space:  global
        .offset:         96
        .size:           8
        .value_kind:     global_buffer
      - .actual_access:  write_only
        .address_space:  global
        .offset:         104
        .size:           8
        .value_kind:     global_buffer
      - .actual_access:  write_only
        .address_space:  global
        .offset:         112
        .size:           8
        .value_kind:     global_buffer
      - .actual_access:  write_only
        .address_space:  global
        .offset:         120
        .size:           8
        .value_kind:     global_buffer
      - .actual_access:  write_only
        .address_space:  global
        .offset:         128
        .size:           8
        .value_kind:     global_buffer
    .group_segment_fixed_size: 121344
    .kernarg_segment_align: 8
    .kernarg_segment_size: 136
    .language:       OpenCL C
    .language_version:
      - 2
      - 0
    .max_flat_workgroup_size: 512
    .name:           _Z11prep_kernelPKfS0_S0_S0_S0_S0_S0_S0_S0_PKiPDv8_DF16bS4_PfS5_S5_PiPt
    .private_segment_fixed_size: 0
    .sgpr_count:     31
    .sgpr_spill_count: 0
    .symbol:         _Z11prep_kernelPKfS0_S0_S0_S0_S0_S0_S0_S0_PKiPDv8_DF16bS4_PfS5_S5_PiPt.kd
    .uniform_work_group_size: 1
    .uses_dynamic_stack: false
    .vgpr_count:     164
    .vgpr_spill_count: 0
    .wavefront_size: 64
  - .agpr_count:     0
    .args:
      - .actual_access:  read_only
        .address_space:  global
        .offset:         0
        .size:           8
        .value_kind:     global_buffer
      - .actual_access:  read_only
        .address_space:  global
        .offset:         8
        .size:           8
        .value_kind:     global_buffer
      - .actual_access:  read_only
        .address_space:  global
        .offset:         16
        .size:           8
        .value_kind:     global_buffer
      - .actual_access:  read_only
        .address_space:  global
        .offset:         24
        .size:           8
        .value_kind:     global_buffer
      - .actual_access:  read_only
        .address_space:  global
        .offset:         32
        .size:           8
        .value_kind:     global_buffer
      - .actual_access:  read_only
        .address_space:  global
        .offset:         40
        .size:           8
        .value_kind:     global_buffer
      - .actual_access:  read_only
        .address_space:  global
        .offset:         48
        .size:           8
        .value_kind:     global_buffer
      - .actual_access:  read_only
        .address_space:  global
        .offset:         56
        .size:           8
        .value_kind:     global_buffer
      - .actual_access:  read_only
        .address_space:  global
        .offset:         64
        .size:           8
        .value_kind:     global_buffer
      - .actual_access:  write_only
        .address_space:  global
        .offset:         72
        .size:           8
        .value_kind:     global_buffer
    .group_segment_fixed_size: 70400
    .kernarg_segment_align: 8
    .kernarg_segment_size: 80
    .language:       OpenCL C
    .language_version:
      - 2
      - 0
    .max_flat_workgroup_size: 512
    .name:           _Z11main_kernelPKDv8_DF16bS1_PKfS3_S3_PKiPKtS3_S3_Pf
    .private_segment_fixed_size: 0
    .sgpr_count:     54
    .sgpr_spill_count: 0
    .symbol:         _Z11main_kernelPKDv8_DF16bS1_PKfS3_S3_PKiPKtS3_S3_Pf.kd
    .uniform_work_group_size: 1
    .uses_dynamic_stack: false
    .vgpr_count:     204
    .vgpr_spill_count: 0
    .wavefront_size: 64
